# attention P.V block: the per-group lgkmcnt(0) replaced by counted lgkmcnt(6..0) waits at each MFMA's own transposed-V read pair (transition waits moved to first consumer)
# speedup vs baseline: 1.0106x; 1.0031x over previous
; #define SBAR() __builtin_amdgcn_sched_barrier(0)
; #define SWRITE_B(b) do { LAS char* vb_ = V_lds + (b) * SHM_V2 + vst00; *(LAS bf16x8*)(vb_ + 16384) = sa0; *(LAS bf16x8*)(vb_ + 18432) = sa1; } while (0)
; template <int D0> __device__ __forceinline__ void pv_one256(f32x16& od, int vb, bf16x8 pa0, bf16x8 pa1, bf16x8 pa2, bf16x8 pa3) {
;   const s16x4 l0 = tr_read<v_rd_off256(D0, 0, 0)>(vb), h0 = tr_read<v_rd_off256(D0, 0, 1)>(vb), l1 = tr_read<v_rd_off256(D0, 1, 0)>(vb), h1 = tr_read<v_rd_off256(D0, 1, 1)>(vb);
;   const s16x4 l2 = tr_read<v_rd_off256(D0, 2, 0)>(vb), h2 = tr_read<v_rd_off256(D0, 2, 1)>(vb), l3 = tr_read<v_rd_off256(D0, 3, 0)>(vb), h3 = tr_read<v_rd_off256(D0, 3, 1)>(vb);
;   asm volatile("s_waitcnt lgkmcnt(0)" ::: "memory"); SBAR();
;     ...
;   od = __builtin_amdgcn_mfma_f32_32x32x16_bf16(pa0, PK(l0, h0), od, 0, 0, 0);
;   od = __builtin_amdgcn_mfma_f32_32x32x16_bf16(pa1, PK(l1, h1), od, 0, 0, 0);
;   od = __builtin_amdgcn_mfma_f32_32x32x16_bf16(pa2, PK(l2, h2), od, 0, 0, 0);
;   od = __builtin_amdgcn_mfma_f32_32x32x16_bf16(pa3, PK(l3, h3), od, 0, 0, 0);
; template <int LDQ, int LDK, int LDO>
; __device__ __forceinline__ void attn_body256(const bf16_t* __restrict__ Qb, const bf16_t* __restrict__ Kh, const bf16_t* __restrict__ Vh, float* __restrict__ Ob, int seq, LAS char* lds) {
;     ...
;     { const int vb = vb0 + (j & 1) * SHM_V2;
;       pv_one256<0>(o[0], vb, pa0, pa1, pa2, pa3); pv_one256<1>(o[1], vb, pa0, pa1, pa2, pa3); pv_one256<2>(o[2], vb, pa0, pa1, pa2, pa3); pv_one256<3>(o[3], vb, pa0, pa1, pa2, pa3);
;       pv_one256<4>(o[4], vb, pa0, pa1, pa2, pa3); pv_one256<5>(o[5], vb, pa0, pa1, pa2, pa3); pv_one256<6>(o[6], vb, pa0, pa1, pa2, pa3); pv_one256<7>(o[7], vb, pa0, pa1, pa2, pa3); }
;     if (j + 1 < NT) { asm volatile("s_waitcnt vmcnt(0)" ::: "memory"); SWRITE_B((j + 1) & 1); }
.LBB0_942:
	v_lshl_add_u32 v0, s88, 15, v244
	ds_read_b64_tr_b16 v[148:149], v0 offset:0
	ds_read_b64_tr_b16 v[150:151], v0 offset:0x1000
	ds_read_b64_tr_b16 v[152:153], v0 offset:0x2000
	ds_read_b64_tr_b16 v[154:155], v0 offset:0x3000
	ds_read_b64_tr_b16 v[156:157], v0 offset:0x4000
	ds_read_b64_tr_b16 v[158:159], v0 offset:0x5000
	ds_read_b64_tr_b16 v[160:161], v0 offset:0x6000
	ds_read_b64_tr_b16 v[162:163], v0 offset:0x7000
	s_nop 0
	s_waitcnt lgkmcnt(6)
	v_mfma_f32_32x32x16_bf16 v[116:131], v[132:135], v[148:151], v[116:131]
	ds_read_b64_tr_b16 v[148:149], v0 offset:0x200
	ds_read_b64_tr_b16 v[150:151], v0 offset:0x1200
	s_waitcnt lgkmcnt(6)
	v_mfma_f32_32x32x16_bf16 v[116:131], v[136:139], v[152:155], v[116:131]
	ds_read_b64_tr_b16 v[152:153], v0 offset:0x2200
	ds_read_b64_tr_b16 v[154:155], v0 offset:0x3200
	s_waitcnt lgkmcnt(6)
	v_mfma_f32_32x32x16_bf16 v[116:131], v[140:143], v[156:159], v[116:131]
	ds_read_b64_tr_b16 v[156:157], v0 offset:0x4200
	ds_read_b64_tr_b16 v[158:159], v0 offset:0x5200
	s_waitcnt lgkmcnt(6)
	v_mfma_f32_32x32x16_bf16 v[116:131], v[144:147], v[160:163], v[116:131]
	ds_read_b64_tr_b16 v[160:161], v0 offset:0x6200
	ds_read_b64_tr_b16 v[162:163], v0 offset:0x7200
	s_waitcnt lgkmcnt(6)
	v_mfma_f32_32x32x16_bf16 v[100:115], v[132:135], v[148:151], v[100:115]
	ds_read_b64_tr_b16 v[148:149], v0 offset:0x400
	ds_read_b64_tr_b16 v[150:151], v0 offset:0x1400
	s_waitcnt lgkmcnt(6)
	v_mfma_f32_32x32x16_bf16 v[100:115], v[136:139], v[152:155], v[100:115]
	ds_read_b64_tr_b16 v[152:153], v0 offset:0x2400
	ds_read_b64_tr_b16 v[154:155], v0 offset:0x3400
	s_waitcnt lgkmcnt(6)
	v_mfma_f32_32x32x16_bf16 v[100:115], v[140:143], v[156:159], v[100:115]
	ds_read_b64_tr_b16 v[156:157], v0 offset:0x4400
	ds_read_b64_tr_b16 v[158:159], v0 offset:0x5400
	s_waitcnt lgkmcnt(6)
	v_mfma_f32_32x32x16_bf16 v[100:115], v[144:147], v[160:163], v[100:115]
	ds_read_b64_tr_b16 v[160:161], v0 offset:0x6400
	ds_read_b64_tr_b16 v[162:163], v0 offset:0x7400
	s_waitcnt lgkmcnt(6)
	v_mfma_f32_32x32x16_bf16 v[84:99], v[132:135], v[148:151], v[84:99]
	ds_read_b64_tr_b16 v[148:149], v0 offset:0x600
	ds_read_b64_tr_b16 v[150:151], v0 offset:0x1600
	s_waitcnt lgkmcnt(6)
	v_mfma_f32_32x32x16_bf16 v[84:99], v[136:139], v[152:155], v[84:99]
	ds_read_b64_tr_b16 v[152:153], v0 offset:0x2600
	ds_read_b64_tr_b16 v[154:155], v0 offset:0x3600
	s_waitcnt lgkmcnt(6)
	v_mfma_f32_32x32x16_bf16 v[84:99], v[140:143], v[156:159], v[84:99]
	ds_read_b64_tr_b16 v[156:157], v0 offset:0x4600
	ds_read_b64_tr_b16 v[158:159], v0 offset:0x5600
	s_waitcnt lgkmcnt(6)
	v_mfma_f32_32x32x16_bf16 v[84:99], v[144:147], v[160:163], v[84:99]
	ds_read_b64_tr_b16 v[160:161], v0 offset:0x6600
	ds_read_b64_tr_b16 v[162:163], v0 offset:0x7600
	s_waitcnt lgkmcnt(6)
	v_mfma_f32_32x32x16_bf16 v[68:83], v[132:135], v[148:151], v[68:83]
	ds_read_b64_tr_b16 v[148:149], v0 offset:0x800
	ds_read_b64_tr_b16 v[150:151], v0 offset:0x1800
	s_waitcnt lgkmcnt(6)
	v_mfma_f32_32x32x16_bf16 v[68:83], v[136:139], v[152:155], v[68:83]
	ds_read_b64_tr_b16 v[152:153], v0 offset:0x2800
	ds_read_b64_tr_b16 v[154:155], v0 offset:0x3800
	s_waitcnt lgkmcnt(6)
	v_mfma_f32_32x32x16_bf16 v[68:83], v[140:143], v[156:159], v[68:83]
	ds_read_b64_tr_b16 v[156:157], v0 offset:0x4800
	ds_read_b64_tr_b16 v[158:159], v0 offset:0x5800
	s_waitcnt lgkmcnt(6)
	v_mfma_f32_32x32x16_bf16 v[68:83], v[144:147], v[160:163], v[68:83]
	ds_read_b64_tr_b16 v[160:161], v0 offset:0x6800
	ds_read_b64_tr_b16 v[162:163], v0 offset:0x7800
	s_waitcnt lgkmcnt(6)
	v_mfma_f32_32x32x16_bf16 v[52:67], v[132:135], v[148:151], v[52:67]
	ds_read_b64_tr_b16 v[148:149], v0 offset:0xa00
	ds_read_b64_tr_b16 v[150:151], v0 offset:0x1a00
	s_waitcnt lgkmcnt(6)
	v_mfma_f32_32x32x16_bf16 v[52:67], v[136:139], v[152:155], v[52:67]
	ds_read_b64_tr_b16 v[152:153], v0 offset:0x2a00
	ds_read_b64_tr_b16 v[154:155], v0 offset:0x3a00
	s_waitcnt lgkmcnt(6)
	v_mfma_f32_32x32x16_bf16 v[52:67], v[140:143], v[156:159], v[52:67]
	ds_read_b64_tr_b16 v[156:157], v0 offset:0x4a00
	ds_read_b64_tr_b16 v[158:159], v0 offset:0x5a00
	s_waitcnt lgkmcnt(6)
	v_mfma_f32_32x32x16_bf16 v[52:67], v[144:147], v[160:163], v[52:67]
	ds_read_b64_tr_b16 v[160:161], v0 offset:0x6a00
	ds_read_b64_tr_b16 v[162:163], v0 offset:0x7a00
	s_waitcnt lgkmcnt(6)
	v_mfma_f32_32x32x16_bf16 v[36:51], v[132:135], v[148:151], v[36:51]
	ds_read_b64_tr_b16 v[148:149], v0 offset:0xc00
	ds_read_b64_tr_b16 v[150:151], v0 offset:0x1c00
	s_waitcnt lgkmcnt(6)
	v_mfma_f32_32x32x16_bf16 v[36:51], v[136:139], v[152:155], v[36:51]
	ds_read_b64_tr_b16 v[152:153], v0 offset:0x2c00
	ds_read_b64_tr_b16 v[154:155], v0 offset:0x3c00
	s_waitcnt lgkmcnt(6)
	v_mfma_f32_32x32x16_bf16 v[36:51], v[140:143], v[156:159], v[36:51]
	ds_read_b64_tr_b16 v[156:157], v0 offset:0x4c00
	ds_read_b64_tr_b16 v[158:159], v0 offset:0x5c00
	s_waitcnt lgkmcnt(6)
	v_mfma_f32_32x32x16_bf16 v[36:51], v[144:147], v[160:163], v[36:51]
	ds_read_b64_tr_b16 v[160:161], v0 offset:0x6c00
	ds_read_b64_tr_b16 v[162:163], v0 offset:0x7c00
	s_waitcnt lgkmcnt(6)
	v_mfma_f32_32x32x16_bf16 v[20:35], v[132:135], v[148:151], v[20:35]
	ds_read_b64_tr_b16 v[148:149], v0 offset:0xe00
	ds_read_b64_tr_b16 v[150:151], v0 offset:0x1e00
	s_waitcnt lgkmcnt(6)
	v_mfma_f32_32x32x16_bf16 v[20:35], v[136:139], v[152:155], v[20:35]
	ds_read_b64_tr_b16 v[152:153], v0 offset:0x2e00
	ds_read_b64_tr_b16 v[154:155], v0 offset:0x3e00
	s_waitcnt lgkmcnt(6)
	v_mfma_f32_32x32x16_bf16 v[20:35], v[140:143], v[156:159], v[20:35]
	ds_read_b64_tr_b16 v[156:157], v0 offset:0x4e00
	ds_read_b64_tr_b16 v[158:159], v0 offset:0x5e00
	s_waitcnt lgkmcnt(6)
	v_mfma_f32_32x32x16_bf16 v[20:35], v[144:147], v[160:163], v[20:35]
	ds_read_b64_tr_b16 v[160:161], v0 offset:0x6e00
	ds_read_b64_tr_b16 v[162:163], v0 offset:0x7e00
	s_waitcnt lgkmcnt(6)
	v_mfma_f32_32x32x16_bf16 v[4:19], v[132:135], v[148:151], v[4:19]
	s_and_b64 vcc, exec, s[8:9]
	s_waitcnt lgkmcnt(4)
	v_mfma_f32_32x32x16_bf16 v[4:19], v[136:139], v[152:155], v[4:19]
	s_waitcnt lgkmcnt(2)
	v_mfma_f32_32x32x16_bf16 v[4:19], v[140:143], v[156:159], v[4:19]
	s_waitcnt lgkmcnt(0)
	v_mfma_f32_32x32x16_bf16 v[4:19], v[144:147], v[160:163], v[4:19]
	s_cbranch_vccnz .LBB0_944
	s_waitcnt vmcnt(0)
	s_and_b32 s8, s86, 0x8000
	v_add_u32_e32 v0, s8, v241
	s_waitcnt vmcnt(1)
	ds_write_b128 v0, v[204:207] offset:16384
	s_waitcnt vmcnt(0)
	ds_write_b128 v0, v[208:211] offset:18432
